# phase B rows: next row loads prefetched one row ahead, norm gains loaded once (on v11)
# baseline (speedup 1.0000x reference)
; #define LAS __attribute__((address_space(3)))
; __device__ __forceinline__ int opaque_tid() { int t = threadIdx.x; asm volatile("" : "+v"(t)); return t; }
; __device__ __forceinline__ unsigned char* opaque_ptr(unsigned char* q) { long z = 0; asm volatile("" : "+s"(z)); return q + z; }
; template <bool MAIN, bool CONV>
; __device__ __forceinline__ void b_row(const Params& p, unsigned char* ws, int l, int row, int lane) {
;     ...
;     if (MAIN) {
;         if (lane < 48) vq = *(const u32x4*)(pr + C_CQ + lane * 8);
;         vkv = *(const u32x2*)(pr + C_CKV + lane * 4);
;         vkr = pr[C_KR + lane];
;         vs5 = *(const u32x4*)(pr + C_S5 + lane * 8);
;         if (lane < 48) { const float* g = p.in[I_QNG] + l * 384 + lane * 8; gq0 = *(const f32x4*)g; gq1 = *(const f32x4*)(g + 4); }
;         gkv = *(const f32x4*)(p.in[I_KVNG] + l * 256 + lane * 4);
;         if (lat) { const int pos = lane >= 32 ? (t & 63) : (t >> 6); rope = ((const f32x2*)(ws + WS_ROPE))[pos * 16 + (lane & 15)]; }
; __device__ __forceinline__ void ph_rowsplit(const Params& p, int l, LAS unsigned char* lds) {
;     const int tid = opaque_tid(), lane = tid & 63, wave = tid >> 6;
;     unsigned char* ws = opaque_ptr(p.ws);
;     const bf16_t* P = (const bf16_t*)(ws + WS_PA);
;     bf16_t* CAT = (bf16_t*)(ws + WS_CAT);
;     const int nsgu = gridDim.x == 256 ? 0 : ((l == 0) ? B_SGU : 256);
;     const int G_ = (int)gridDim.x, c_ = (int)blockIdx.x, nx = nsgu > G_ ? nsgu - G_ : 0;
;     const bool bal = nx > 0 && nx < G_ && nsgu <= 2 * G_;
;     const int nfew = bal ? 2 * nx : 0;
;     const int nmine = (c_ < nsgu ? 1 : 0) + (c_ < nx ? 1 : 0);
;     int rit = bal ? (c_ < nx ? c_ : nfew + (c_ - nx)) : c_; const int rstride = bal ? (c_ < nx ? nx : G_ - nx) : G_; const int rend = bal ? (c_ < nx ? nfew : B_ROWITEMS) : B_ROWITEMS;
;     for (int k = 0; ; ++k) {
;         int it;
;         if (k < nmine) it = B_ROWITEMS + c_ + k * G_;
;         else { if (rit >= rend) break; it = rit; rit += rstride; }
;         if (it < B_ROWITEMS) {
;             const int row = it * 8 + wave;
;             if (gridDim.x == 256) b_row<true, false>(p, ws, l, row, lane); else b_row<true, true>(p, ws, l, row, lane);
.LBB0_465:
	s_andn2_b64 vcc, exec, s[0:1]
	v_readlane_b32 s0, v252, 5
	v_readlane_b32 s1, v252, 6
	s_mov_b32 s1, s5
	v_writelane_b32 v252, s0, 5
	s_nop 1
	v_writelane_b32 v252, s1, 6
	s_cbranch_vccnz .LBB0_590
	v_readlane_b32 s0, v252, 20
	v_readlane_b32 s1, v252, 21
	s_and_b64 s[0:1], s[0:1], exec
	s_movk_i32 s0, 0x120
	s_cselect_b32 s2, s0, 0x100
	v_readlane_b32 s0, v251, 50
	v_readlane_b32 s1, v251, 51
	s_and_b64 s[0:1], s[0:1], exec
	s_cselect_b32 s4, 0, s2
	s_sub_i32 s0, s4, s94
	s_cmp_gt_i32 s4, s94
	s_cselect_b32 s13, s0, 0
	s_cmp_lt_i32 s13, 1
	s_cselect_b64 s[0:1], -1, 0
	s_cmp_le_i32 s94, s13
	s_cselect_b64 s[2:3], -1, 0
	s_or_b64 s[0:1], s[0:1], s[2:3]
	v_readlane_b32 s2, v253, 18
	s_cmp_gt_u32 s4, s2
	s_cselect_b64 s[2:3], -1, 0
	s_or_b64 s[0:1], s[0:1], s[2:3]
	s_lshl_b32 s14, s13, 1
	s_and_b64 s[2:3], s[0:1], exec
	s_cselect_b32 s14, 0, s14
	s_cmp_lt_i32 s92, s13
	s_cselect_b64 s[2:3], -1, 0
	s_and_b64 s[2:3], s[2:3], exec
	s_cselect_b32 s15, s14, 0x480
	s_sub_i32 s16, s94, s13
	s_cmp_lt_i32 s92, s13
	s_cselect_b64 vcc, -1, 0
	s_and_b64 s[2:3], vcc, exec
	s_cselect_b32 s16, s13, s16
	s_cmp_lt_i32 s92, s4
	s_cselect_b64 s[2:3], -1, 0
	s_waitcnt vmcnt(0)
	v_cndmask_b32_e64 v2, 0, 1, s[2:3]
	v_addc_co_u32_e64 v75, s[2:3], 0, v2, vcc
	s_sub_i32 s4, s92, s13
	s_or_b64 s[2:3], vcc, s[0:1]
	s_add_i32 s4, s4, s14
	s_and_b64 s[2:3], s[2:3], exec
	s_cselect_b32 s31, s92, s4
	s_and_b64 s[0:1], s[0:1], exec
	v_readlane_b32 s2, v252, 5
	s_cselect_b32 s13, s94, s16
	s_cselect_b32 s24, 0x480, s15
	s_lshl_b32 s18, s2, 9
	s_mov_b32 s19, s5
	v_readlane_b32 s52, v251, 16
	s_lshl_b32 s0, s2, 8
	s_lshl_b64 s[14:15], s[18:19], 2
	v_readlane_b32 s56, v251, 20
	s_mul_i32 s4, s2, 0x180
	v_readlane_b32 s57, v251, 21
	s_add_u32 s25, s56, s14
	v_readlane_b32 s62, v251, 26
	s_addc_u32 s26, s57, s15
	s_lshl_b64 s[14:15], s[4:5], 2
	s_mov_b32 s1, s5
	v_readlane_b32 s63, v251, 27
	s_add_u32 s14, s62, s14
	v_readlane_b32 s3, v252, 6
	v_readlane_b32 s66, v251, 30
	s_addc_u32 s15, s63, s15
	s_lshl_b64 s[0:1], s[0:1], 2
	s_mulk_i32 s2, 0x600
	s_mov_b32 s3, s5
	v_readlane_b32 s67, v251, 31
	s_add_u32 s0, s66, s0
	v_readlane_b32 s36, v251, 32
	s_addc_u32 s1, s67, s1
	s_lshl_b64 s[2:3], s[2:3], 2
	v_readlane_b32 s42, v251, 38
	v_readlane_b32 s43, v251, 39
	s_add_u32 s2, s42, s2
	s_addc_u32 s3, s43, s3
	v_mov_b32_e32 v4, v0
	s_mov_b64 s[16:17], 0
	s_add_u32 s20, s84, s16
	v_and_b32_e32 v74, 63, v4
	s_addc_u32 s21, s85, s17
	v_lshlrev_b32_e32 v76, 3, v74
	v_mov_b32_e32 v77, v207
	s_add_u32 s22, s20, 0x1f1b8000
	v_lshl_add_u64 v[2:3], s[20:21], 0, v[76:77]
	s_mov_b64 s[16:17], 0x2fc78000
	v_readlane_b32 s40, v251, 36
	v_readlane_b32 s41, v251, 37
	s_addc_u32 s23, s21, 0
	v_lshl_add_u64 v[80:81], v[2:3], 0, s[16:17]
	v_and_b32_e32 v2, 16, v4
	v_lshlrev_b32_e32 v206, 1, v74
	s_add_u32 s34, s20, 0x3d740000
	v_cmp_eq_u32_e64 s[40:41], 0, v2
	v_lshl_add_u64 v[2:3], s[20:21], 0, v[206:207]
	s_mov_b64 s[16:17], 0x30e78100
	v_ashrrev_i32_e32 v79, 6, v4
	s_addc_u32 s35, s21, 0
	v_and_b32_e32 v89, 15, v4
	v_lshl_add_u64 v[82:83], v[2:3], 0, s[16:17]
	v_bfe_u32 v4, v4, 1, 5
	v_lshlrev_b32_e32 v2, 5, v74
	v_mov_b32_e32 v3, v207
	v_lshlrev_b32_e32 v206, 4, v74
	v_readlane_b32 s37, v251, 33
	v_readlane_b32 s38, v251, 34
	v_readlane_b32 s39, v251, 35
	v_lshl_add_u64 v[84:85], s[14:15], 0, v[2:3]
	s_add_u32 s16, s20, 0x324f8000
	v_mul_u32_u24_e32 v86, 0x300, v4
	v_lshl_add_u64 v[4:5], s[20:21], 0, v[206:207]
	s_mov_b64 s[14:15], 0x2f5b8000
	v_lshl_add_u64 v[92:93], s[0:1], 0, v[206:207]
	v_lshl_add_u64 v[94:95], s[2:3], 0, v[2:3]
	s_mov_b64 s[0:1], 0x1000
	s_mov_b32 s12, 0
	v_cmp_gt_u32_e64 s[36:37], 48, v74
	v_lshlrev_b32_e32 v78, 2, v74
	v_cmp_lt_u32_e64 s[38:39], 31, v74
	s_addc_u32 s17, s21, 0
	v_mov_b32_e32 v87, v207
	v_and_b32_e32 v88, 8, v76
	v_lshl_add_u64 v[90:91], v[4:5], 0, s[14:15]
	v_lshl_add_u64 v[96:97], v[94:95], 0, s[0:1]
	v_readlane_b32 s27, v255, 30
	v_readlane_b32 s53, v251, 17
	v_readlane_b32 s54, v251, 18
	v_readlane_b32 s55, v251, 19
	v_readlane_b32 s58, v251, 22
	v_readlane_b32 s59, v251, 23
	v_readlane_b32 s60, v251, 24
	v_readlane_b32 s61, v251, 25
	v_readlane_b32 s64, v251, 28
	v_readlane_b32 s65, v251, 29
	v_readlane_b32 s44, v251, 40
	v_readlane_b32 s45, v251, 41
	v_readlane_b32 s46, v251, 42
	v_readlane_b32 s47, v251, 43
	v_readlane_b32 s48, v251, 44
	v_readlane_b32 s49, v251, 45
	v_readlane_b32 s50, v251, 46
	v_readlane_b32 s51, v251, 47
	v_mov_b32_e32 v192, 0
	v_mov_b32_e32 v193, 0
	v_mov_b32_e32 v194, 0
	v_mov_b32_e32 v195, 0
	v_mov_b32_e32 v196, 0
	v_mov_b32_e32 v197, 0
	v_mov_b32_e32 v198, 0
	v_mov_b32_e32 v199, 0
	s_and_saveexec_b64 s[0:1], s[36:37]
	global_load_dwordx4 v[192:195], v[84:85], off offset:16
	global_load_dwordx4 v[196:199], v[84:85], off
	s_or_b64 exec, exec, s[0:1]
	global_load_dwordx4 v[200:203], v[92:93], off
	v_lshl_add_u32 v170, s31, 3, v79
	v_mov_b64_e32 v[172:173], s[22:23]
	s_movk_i32 s0, 0x1e00
	v_mad_i64_i32 v[172:173], s[2:3], v170, s0, v[172:173]
	v_mov_b32_e32 v167, v207
	v_lshlrev_b32_e32 v166, 4, v74
	v_lshl_add_u64 v[174:175], v[172:173], 0, v[166:167]
	v_mov_b32_e32 v176, 0
	v_mov_b32_e32 v177, 0
	v_mov_b32_e32 v178, 0
	v_mov_b32_e32 v179, 0
	s_and_saveexec_b64 s[0:1], s[36:37]
	global_load_dwordx4 v[176:179], v[174:175], off offset:2048
	s_or_b64 exec, exec, s[0:1]
	global_load_dwordx4 v[184:187], v[174:175], off offset:3456
	v_lshlrev_b32_e32 v166, 3, v74
	v_lshl_add_u64 v[174:175], v[172:173], 0, v[166:167]
	global_load_dwordx2 v[180:181], v[174:175], off offset:2816
	v_lshlrev_b32_e32 v166, 1, v74
	v_lshl_add_u64 v[174:175], v[172:173], 0, v[166:167]
	global_load_ushort v182, v[174:175], off offset:3328
	v_mov_b32_e32 v188, 1.0
	v_mov_b32_e32 v189, 0
	s_movk_i32 s2, 0x2000
	v_cmp_gt_i32_e64 s[0:1], s2, v170
	v_and_b32_e32 v168, 63, v170
	v_and_b32_e32 v169, 0x7ff, v170
	v_lshrrev_b32_e32 v169, 6, v169
	v_cndmask_b32_e64 v168, v169, v168, s[38:39]
	v_lshlrev_b32_e32 v169, 3, v89
	v_lshl_or_b32 v168, v168, 7, v169
	s_and_saveexec_b64 s[2:3], s[0:1]
	global_load_dwordx2 v[188:189], v168, s[34:35]
	s_or_b64 exec, exec, s[2:3]
	s_waitcnt vmcnt(0)
	s_branch .LBB0_469
; __device__ __forceinline__ unsigned cvt_pk_bf16(float lo, float hi) { const f32x2 v = {lo, hi}; const bf16x2_t b = __builtin_convertvector(v, bf16x2_t); return __builtin_bit_cast(unsigned, b); }
; __device__ __forceinline__ float bf2f(unsigned short b) { return __uint_as_float(((unsigned)b) << 16); }
; __device__ __forceinline__ float bflo(unsigned w) { return __uint_as_float(w << 16); }
; __device__ __forceinline__ float bfhi(unsigned w) { return __uint_as_float(w & 0xffff0000u); }
; __device__ __forceinline__ unsigned short f2bf(float f) { return (unsigned short)(cvt_pk_bf16(f, 0.f) & 0xffffu); }
; template <bool MAIN, bool CONV>
; __device__ __forceinline__ void b_row(const Params& p, unsigned char* ws, int l, int row, int lane) {
;     ...
;         { const u32x2 v = vkv; const float f0 = bflo(v.x), f1 = bfhi(v.x), f2 = bflo(v.y), f3 = bfhi(v.y);
;           const float ss = wave_sum(f0 * f0 + f1 * f1 + f2 * f2 + f3 * f3); const float rinv = rsqrtf(ss * (1.0f / 256.0f) + EPS);
;           u32x2 w; w.x = cvt_pk_bf16(f0 * rinv * gkv[0], f1 * rinv * gkv[1]); w.y = cvt_pk_bf16(f2 * rinv * gkv[2], f3 * rinv * gkv[3]);
;           *(u32x2*)((bf16_t*)(ws + WS_KVA) + (size_t)row * 256 + lane * 4) = w; }
;         { float v = bf2f(vkr); const float partner = __shfl_xor(v, 16);
;           if (lat) { const int jj = lane & 31; const float cs = rope.x, sn = rope.y;
;               v = jj < 16 ? (v * cs - partner * sn) : (v * cs + partner * sn); }
;           const int key = lat ? CTX + t : t; const unsigned short o = f2bf(v);
;           bf16_t* kc = (bf16_t*)(ws + WS_KC);
;     #pragma unroll
;           for (int h = 0; h < 4; ++h) kc[((size_t)(b * 4 + h) * NKEY + key) * 192 + 128 + lane] = o; }
;         { const u32x4 v = vs5; const int g = lane >> 1, half = lane & 1;
;           *(u32x4*)((bf16_t*)(ws + WS_UPK) + ((size_t)g * 768 + (row >> 4)) * 512 + (row & 15) * 16 + half * 8) = v; }
.LBB0_467:
	s_or_b64 exec, exec, s[0:1]
	v_add_u32_e32 v7, 0xffffe000, v98
	v_ashrrev_i32_e32 v6, 11, v98
	v_lshrrev_b32_e32 v7, 8, v7
	v_lshlrev_b32_e32 v14, 16, v24
	v_and_b32_e32 v15, 0xffff0000, v24
	v_cndmask_b32_e64 v26, v7, v6, s[42:43]
	v_lshlrev_b32_e32 v6, 16, v25
	v_and_b32_e32 v7, 0xffff0000, v25
	v_pk_mul_f32 v[16:17], v[14:15], v[14:15]
	v_pk_mul_f32 v[8:9], v[6:7], v[6:7]
	v_add_f32_e32 v16, v16, v17
	v_add_f32_e32 v8, v8, v16
	v_add_f32_e32 v8, v9, v8
	ds_bpermute_b32 v9, v19, v8
	s_mov_b32 s0, 0x800000
	v_and_b32_e32 v27, 0xff, v98
	s_movk_i32 s3, 0x900
	s_movk_i32 s2, 0x180
	s_waitcnt lgkmcnt(0)
	v_add_f32_e32 v8, v8, v9
	ds_bpermute_b32 v9, v18, v8
	s_waitcnt lgkmcnt(0)
	v_add_f32_e32 v8, v8, v9
	ds_bpermute_b32 v9, v20, v8
	s_waitcnt lgkmcnt(0)
	v_add_f32_e32 v8, v8, v9
	ds_bpermute_b32 v9, v21, v8
	s_waitcnt lgkmcnt(0)
	v_add_f32_e32 v8, v8, v9
	ds_bpermute_b32 v9, v35, v8
	s_waitcnt lgkmcnt(0)
	v_add_f32_e32 v8, v8, v9
	ds_bpermute_b32 v9, v36, v8
	s_waitcnt lgkmcnt(0)
	v_add_f32_e32 v8, v8, v9
	v_fmamk_f32 v8, v8, 0x3b800000, v246
	v_cmp_gt_f32_e32 vcc, s0, v8
	v_mul_f32_e32 v9, 0x4b800000, v8
	s_nop 0
	v_cndmask_b32_e32 v8, v8, v9, vcc
	v_rsq_f32_e32 v8, v8
	s_nop 0
	v_mul_f32_e32 v9, 0x45800000, v8
	v_cndmask_b32_e32 v8, v8, v9, vcc
	v_pk_mul_f32 v[14:15], v[8:9], v[14:15] op_sel_hi:[0,1]
	v_pk_mul_f32 v[6:7], v[8:9], v[6:7] op_sel_hi:[0,1]
	v_pk_mul_f32 v[10:11], v[10:11], v[14:15]
	v_pk_mul_f32 v[6:7], v[12:13], v[6:7]
	v_cvt_pk_bf16_f32 v10, v10, v11
	v_cvt_pk_bf16_f32 v11, v6, v7
	v_lshlrev_b64 v[6:7], 9, v[98:99]
	v_lshl_add_u64 v[6:7], v[80:81], 0, v[6:7]
	global_store_dwordx2 v[6:7], v[10:11], off
	v_lshlrev_b32_e32 v6, 16, v34
	ds_bpermute_b32 v7, v18, v6
	v_lshlrev_b32_e32 v11, 2, v26
	s_waitcnt lgkmcnt(0)
	v_mul_f32_e32 v7, v23, v7
	v_cndmask_b32_e64 v7, v7, -v7, s[40:41]
	v_fmac_f32_e32 v7, v22, v6
	v_cndmask_b32_e64 v6, v6, v7, s[42:43]
	v_add_u32_e32 v7, 0x100, v77
	v_cndmask_b32_e64 v206, v27, v7, s[42:43]
	v_cvt_pk_bf16_f32 v10, v6, s0
	v_mad_i64_i32 v[6:7], s[0:1], v11, s3, v[206:207]
	v_mad_u64_u32 v[8:9], s[0:1], v6, s2, v[82:83]
	v_or_b32_e32 v6, 1, v11
	v_mad_i32_i24 v9, v7, s2, v9
	v_mad_i64_i32 v[6:7], s[0:1], v6, s3, v[206:207]
	global_store_short v[8:9], v10, off
	v_mad_u64_u32 v[8:9], s[0:1], v6, s2, v[82:83]
	v_or_b32_e32 v6, 2, v11
	v_mad_i32_i24 v9, v7, s2, v9
	v_mad_i64_i32 v[6:7], s[0:1], v6, s3, v[206:207]
	global_store_short v[8:9], v10, off
	v_mad_u64_u32 v[8:9], s[0:1], v6, s2, v[82:83]
	v_or_b32_e32 v6, 3, v11
	v_mad_i32_i24 v9, v7, s2, v9
	v_mad_i64_i32 v[6:7], s[0:1], v6, s3, v[206:207]
	global_store_short v[8:9], v10, off
	v_mad_u64_u32 v[8:9], s[0:1], v6, s2, v[82:83]
	v_ashrrev_i32_e32 v6, 4, v98
	v_mad_i32_i24 v9, v7, s2, v9
	v_ashrrev_i32_e32 v7, 31, v6
	v_lshl_add_u64 v[6:7], v[6:7], 0, v[86:87]
	global_store_short v[8:9], v10, off
	v_lshlrev_b64 v[6:7], 10, v[6:7]
	v_lshlrev_b32_e32 v8, 5, v98
	v_lshl_add_u64 v[6:7], s[16:17], 0, v[6:7]
	v_and_b32_e32 v206, 0x1e0, v8
	v_lshl_add_u64 v[6:7], v[6:7], 0, v[206:207]
	v_lshlrev_b32_e32 v206, 1, v88
	v_lshl_add_u64 v[6:7], v[6:7], 0, v[206:207]
	global_store_dwordx4 v[6:7], v[2:5], off

; template <bool MAIN, bool CONV>
; __device__ __forceinline__ void b_row(const Params& p, unsigned char* ws, int l, int row, int lane) {
;     ...
;     if (MAIN) {
;         if (lane < 48) vq = *(const u32x4*)(pr + C_CQ + lane * 8);
;         vkv = *(const u32x2*)(pr + C_CKV + lane * 4);
;         vkr = pr[C_KR + lane];
;         vs5 = *(const u32x4*)(pr + C_S5 + lane * 8);
;         if (lane < 48) { const float* g = p.in[I_QNG] + l * 384 + lane * 8; gq0 = *(const f32x4*)g; gq1 = *(const f32x4*)(g + 4); }
;         gkv = *(const f32x4*)(p.in[I_KVNG] + l * 256 + lane * 4);
;         if (lat) { const int pos = lane >= 32 ? (t & 63) : (t >> 6); rope = ((const f32x2*)(ws + WS_ROPE))[pos * 16 + (lane & 15)]; }
;     }
;     if (CONV) {
;         ca = *(const u32x4*)(pr + C_CVC + c0); ch = *(const u32x4*)(pr + C_CVH + c0); bg = *(const u32x4*)(pr + C_CVB + c0);
;         if (t > 0) { pa = *(const u32x4*)(pr - INP + C_CVC + c0); ph = *(const u32x4*)(pr - INP + C_CVH + c0); }
;         if (t < seqlen - 1) { na = *(const u32x4*)(pr + INP + C_CVC + c0); nh = *(const u32x4*)(pr + INP + C_CVH + c0); }
;         const float* cw = p.in[I_CONVW] + (size_t)l * 3 * 512 + c0;
;         cw0a = *(const f32x4*)cw; cw0b = *(const f32x4*)(cw + 4); cw1a = *(const f32x4*)(cw + 512); cw1b = *(const f32x4*)(cw + 516); cw2a = *(const f32x4*)(cw + 1024); cw2b = *(const f32x4*)(cw + 1028);
;     }
;     asm volatile("" ::: "memory");
;     if (MAIN) {
;         { float f[8]; float ss = 0.f;
;           if (lane < 48) { const u32x4 v = vq; f[0] = bflo(v.x); f[1] = bfhi(v.x); f[2] = bflo(v.y); f[3] = bfhi(v.y); f[4] = bflo(v.z); f[5] = bfhi(v.z); f[6] = bflo(v.w); f[7] = bfhi(v.w);
;     #pragma unroll
;               for (int j = 0; j < 8; ++j) ss += f[j] * f[j]; }
;           else {
;     #pragma unroll
;               for (int j = 0; j < 8; ++j) f[j] = 0.f; }
;           ss = wave_sum(ss); const float rinv = rsqrtf(ss * (1.0f / 384.0f) + EPS);
;           if (lane < 48) { u32x4 w;
;               w.x = cvt_pk_bf16(f[0] * rinv * gq0[0], f[1] * rinv * gq0[1]); w.y = cvt_pk_bf16(f[2] * rinv * gq0[2], f[3] * rinv * gq0[3]);
;               w.z = cvt_pk_bf16(f[4] * rinv * gq1[0], f[5] * rinv * gq1[1]); w.w = cvt_pk_bf16(f[6] * rinv * gq1[2], f[7] * rinv * gq1[3]);
;               *(u32x4*)((bf16_t*)(ws + WS_QA) + (size_t)row * 384 + lane * 8) = w; } }
.LBB0_528:
	s_and_b64 vcc, exec, s[0:1]
	s_cbranch_vccz .LBB0_468
	s_waitcnt vmcnt(7)
	v_mov_b32_e32 v18, v176
	v_mov_b32_e32 v19, v177
	v_mov_b32_e32 v20, v178
	v_mov_b32_e32 v21, v179
	v_mov_b32_e32 v24, v180
	v_mov_b32_e32 v25, v181
	v_mov_b32_e32 v34, v182
	v_mov_b32_e32 v2, v184
	v_mov_b32_e32 v3, v185
	v_mov_b32_e32 v4, v186
	v_mov_b32_e32 v5, v187
	v_mov_b32_e32 v22, v188
	v_mov_b32_e32 v23, v189
	v_mov_b32_e32 v6, v192
	v_mov_b32_e32 v7, v193
	v_mov_b32_e32 v8, v194
	v_mov_b32_e32 v9, v195
	v_mov_b32_e32 v14, v196
	v_mov_b32_e32 v15, v197
	v_mov_b32_e32 v16, v198
	v_mov_b32_e32 v17, v199
	v_mov_b32_e32 v10, v200
	v_mov_b32_e32 v11, v201
	v_mov_b32_e32 v12, v202
	v_mov_b32_e32 v13, v203
	v_mov_b32_e32 v35, 0
	s_cmp_lt_i32 s30, s24
	s_cbranch_scc0 .Lbpf_skip
	v_lshl_add_u32 v170, s30, 3, v79
	v_mov_b64_e32 v[172:173], s[22:23]
	s_movk_i32 s0, 0x1e00
	v_mad_i64_i32 v[172:173], s[2:3], v170, s0, v[172:173]
	v_mov_b32_e32 v167, v207
	v_lshlrev_b32_e32 v166, 4, v74
	v_lshl_add_u64 v[174:175], v[172:173], 0, v[166:167]
	v_mov_b32_e32 v176, 0
	v_mov_b32_e32 v177, 0
	v_mov_b32_e32 v178, 0
	v_mov_b32_e32 v179, 0
	s_and_saveexec_b64 s[0:1], s[36:37]
	global_load_dwordx4 v[176:179], v[174:175], off offset:2048
	s_or_b64 exec, exec, s[0:1]
	global_load_dwordx4 v[184:187], v[174:175], off offset:3456
	v_lshlrev_b32_e32 v166, 3, v74
	v_lshl_add_u64 v[174:175], v[172:173], 0, v[166:167]
	global_load_dwordx2 v[180:181], v[174:175], off offset:2816
	v_lshlrev_b32_e32 v166, 1, v74
	v_lshl_add_u64 v[174:175], v[172:173], 0, v[166:167]
	global_load_ushort v182, v[174:175], off offset:3328
	v_mov_b32_e32 v188, 1.0
	v_mov_b32_e32 v189, 0
	s_movk_i32 s2, 0x2000
	v_cmp_gt_i32_e64 s[0:1], s2, v170
	v_and_b32_e32 v168, 63, v170
	v_and_b32_e32 v169, 0x7ff, v170
	v_lshrrev_b32_e32 v169, 6, v169
	v_cndmask_b32_e64 v168, v169, v168, s[38:39]
	v_lshlrev_b32_e32 v169, 3, v89
	v_lshl_or_b32 v168, v168, 7, v169
	s_and_saveexec_b64 s[2:3], s[0:1]
	global_load_dwordx2 v[188:189], v168, s[34:35]
	s_or_b64 exec, exec, s[2:3]
.Lbpf_skip:
	v_mov_b32_e32 v26, 0
	v_mov_b32_e32 v27, 0
	v_mov_b32_e32 v28, 0
	v_mov_b32_e32 v29, 0
	v_mov_b32_e32 v30, 0
	v_mov_b32_e32 v31, 0
	v_mov_b32_e32 v32, 0
	v_mov_b32_e32 v33, 0
	s_and_saveexec_b64 s[0:1], s[36:37]
	s_cbranch_execz .LBB0_537
	v_lshlrev_b32_e32 v26, 16, v18
	v_and_b32_e32 v27, 0xffff0000, v18
	v_pk_mul_f32 v[36:37], v[26:27], v[26:27]
	v_and_b32_e32 v18, 0xffff0000, v19
	v_lshlrev_b32_e32 v19, 16, v19
	v_pk_mov_b32 v[28:29], v[18:19], v[18:19] op_sel:[1,0]
	v_pk_mul_f32 v[18:19], v[18:19], v[18:19]
	v_add_f32_e32 v35, v36, v37
	v_and_b32_e32 v32, 0xffff0000, v20
	v_lshlrev_b32_e32 v33, 16, v20
	v_add_f32_e32 v19, v19, v35
	v_pk_mul_f32 v[38:39], v[32:33], v[32:33]
	v_add_f32_e32 v18, v18, v19
	v_and_b32_e32 v20, 0xffff0000, v21
	v_lshlrev_b32_e32 v21, 16, v21
	v_add_f32_e32 v18, v39, v18
	v_pk_mov_b32 v[30:31], v[32:33], v[32:33] op_sel:[1,0]
	v_pk_mov_b32 v[32:33], v[20:21], v[20:21] op_sel:[1,0]
	v_pk_mul_f32 v[20:21], v[20:21], v[20:21]
	v_add_f32_e32 v18, v38, v18
	v_add_f32_e32 v18, v21, v18
	v_add_f32_e32 v35, v20, v18
.LBB0_537:
	s_or_b64 exec, exec, s[0:1]
	v_and_b32_e32 v18, 64, v249
	v_add_u32_e32 v36, 64, v18
	v_xor_b32_e32 v18, 32, v249
	v_cmp_lt_i32_e32 vcc, v18, v36
	s_nop 1
	v_cndmask_b32_e32 v18, v249, v18, vcc
	v_lshlrev_b32_e32 v19, 2, v18
	v_mov_b32_e32 v18, v35
	s_nop 1
	v_permlane32_swap_b32_e32 v18, v35
	s_waitcnt lgkmcnt(0)
	v_add_f32_e32 v20, v35, v18
	v_xor_b32_e32 v18, 16, v249
	v_cmp_lt_i32_e32 vcc, v18, v36
	s_nop 1
	v_cndmask_b32_e32 v18, v249, v18, vcc
	v_lshlrev_b32_e32 v18, 2, v18
	v_mov_b32_e32 v21, v20
	s_nop 1
	v_permlane16_swap_b32_e32 v21, v20
	s_waitcnt lgkmcnt(0)
	v_add_f32_e32 v21, v20, v21
	v_xor_b32_e32 v20, 8, v249
	v_cmp_lt_i32_e32 vcc, v20, v36
	s_nop 1
	v_cndmask_b32_e32 v20, v249, v20, vcc
	v_lshlrev_b32_e32 v20, 2, v20
	s_nop 1
	v_mov_b32_dpp v35, v21 row_ror:8 row_mask:0xf bank_mask:0xf
	s_waitcnt lgkmcnt(0)
	v_add_f32_e32 v35, v21, v35
	v_xor_b32_e32 v21, 4, v249
	v_cmp_lt_i32_e32 vcc, v21, v36
	s_nop 1
	v_cndmask_b32_e32 v21, v249, v21, vcc
	v_lshlrev_b32_e32 v21, 2, v21
	s_nop 1
	v_mov_b32_dpp v37, v35 row_shl:4 row_mask:0xf bank_mask:0x5
	v_mov_b32_dpp v37, v35 row_shr:4 row_mask:0xf bank_mask:0xa
	s_waitcnt lgkmcnt(0)
	v_add_f32_e32 v37, v35, v37
	v_xor_b32_e32 v35, 2, v249
	v_cmp_lt_i32_e32 vcc, v35, v36
	s_nop 1
	v_cndmask_b32_e32 v35, v249, v35, vcc
	v_lshlrev_b32_e32 v35, 2, v35
	s_nop 1
	v_mov_b32_dpp v38, v37 quad_perm:[2,3,0,1] row_mask:0xf bank_mask:0xf
	s_waitcnt lgkmcnt(0)
	v_add_f32_e32 v37, v37, v38
	v_xor_b32_e32 v38, 1, v249
	v_cmp_lt_i32_e32 vcc, v38, v36
	s_nop 1
	v_cndmask_b32_e32 v36, v249, v38, vcc
	v_lshlrev_b32_e32 v36, 2, v36
	s_nop 1
	v_mov_b32_dpp v38, v37 quad_perm:[1,0,3,2] row_mask:0xf bank_mask:0xf
	s_and_saveexec_b64 s[0:1], s[36:37]
	s_cbranch_execz .LBB0_467
	s_waitcnt lgkmcnt(0)
	v_add_f32_e32 v37, v37, v38
	v_fmamk_f32 v37, v37, 0x3b2aaaab, v246
	s_mov_b32 s2, 0x800000
	v_mul_f32_e32 v38, 0x4b800000, v37
	v_cmp_gt_f32_e32 vcc, s2, v37
	s_movk_i32 s2, 0x300
	s_nop 0
	v_cndmask_b32_e32 v37, v37, v38, vcc
	v_rsq_f32_e32 v37, v37
	s_nop 0
	v_mul_f32_e32 v38, 0x45800000, v37
	v_cndmask_b32_e32 v38, v37, v38, vcc
	v_pk_mul_f32 v[26:27], v[26:27], v[38:39] op_sel_hi:[1,0]
	v_pk_mul_f32 v[28:29], v[28:29], v[38:39] op_sel_hi:[1,0]
	v_pk_mul_f32 v[14:15], v[14:15], v[26:27]
	v_pk_mul_f32 v[16:17], v[16:17], v[28:29]
	v_cvt_pk_bf16_f32 v14, v14, v15
	v_cvt_pk_bf16_f32 v15, v16, v17
	v_pk_mul_f32 v[16:17], v[30:31], v[38:39] op_sel_hi:[1,0]
	s_nop 0
	v_pk_mul_f32 v[6:7], v[6:7], v[16:17]
	s_nop 0
	v_cvt_pk_bf16_f32 v16, v6, v7
	v_pk_mul_f32 v[6:7], v[32:33], v[38:39] op_sel_hi:[1,0]
	s_nop 0
	v_pk_mul_f32 v[6:7], v[8:9], v[6:7]
	s_nop 0
	v_cvt_pk_bf16_f32 v17, v6, v7
	v_mad_i64_i32 v[6:7], s[2:3], v98, s2, v[90:91]
	global_store_dwordx4 v[6:7], v[14:17], off
	s_branch .LBB0_467
